# speedup vs baseline: 1.0031x; 1.0031x over previous
.LBB2_12:
	s_waitcnt lgkmcnt(0)
	s_mov_b32 s16, 0
	s_mov_b32 s22, s6
	s_mov_b32 s23, s7
	s_mov_b32 s17, s78
	s_nop 0
